# speedup vs baseline: 1.0053x; 1.0053x over previous
_Z11proj_kernelPKfS0_S0_PKDF16_S0_S0_S0_PDF16_S3_S3_Pj:
	s_ashr_i32 s12, s2, 6
	s_load_dwordx8 s[4:11], s[0:1], 0x0
	s_cmp_gt_u32 s2, 63
	s_cselect_b64 s[22:23], -1, 0
	s_cmp_lg_u32 s12, 1
	s_cselect_b64 s[18:19], -1, 0
	s_cmp_eq_u32 s12, 1
	s_cselect_b64 s[20:21], -1, 0
	s_and_b64 s[14:15], s[20:21], exec
	s_waitcnt lgkmcnt(0)
	s_cselect_b32 s14, s6, s8
	s_cselect_b32 s15, s7, s9
	s_ashr_i32 s13, s12, 31
	s_lshl_b32 s28, s2, 7
	s_lshl_b64 s[6:7], s[12:13], 19
	s_and_b32 s3, s28, 0x1f80
	s_cmp_lt_u32 s2, 64
	s_cselect_b64 vcc, -1, 0
	v_lshrrev_b32_e32 v1, 2, v0
	v_lshrrev_b32_e32 v2, 2, v0
	v_and_b32_e32 v2, 0x70, v2
	v_bfe_u32 v254, v0, 3, 3
	v_or_b32_e32 v254, v2, v254
	v_or_b32_e32 v2, s3, v254
	s_and_b64 s[8:9], vcc, exec
	s_cselect_b32 s25, s5, s15
	s_cselect_b32 s24, s4, s14
	v_lshlrev_b32_e32 v2, 11, v2
	v_mov_b32_e32 v3, 0
	v_lshlrev_b32_e32 v6, 4, v0
	s_add_u32 s4, s10, s6
	v_lshl_add_u64 v[4:5], s[24:25], 0, v[2:3]
	v_and_b32_e32 v6, 0x70, v6
	v_mov_b32_e32 v7, v3
	v_lshlrev_b32_e32 v56, 4, v0
	v_mov_b32_e32 v57, v3
	s_addc_u32 s5, s11, s7
	v_lshl_add_u64 v[4:5], v[4:5], 0, v[6:7]
	s_mov_b64 s[46:47], 0x4000
	v_lshl_add_u64 v[250:251], v[4:5], 0, s[46:47]
	s_movk_i32 s8, 0x2000
	v_lshl_add_u64 v[6:7], s[4:5], 0, v[56:57]
	global_load_dwordx4 v[8:11], v[4:5], off sc1 nt
	global_load_dwordx4 v[12:15], v[250:251], off sc1 nt
	global_load_dwordx4 v[16:19], v56, s[4:5] sc0 sc1
	v_add_co_u32_e64 v28, s[4:5], s8, v6
	s_mov_b32 s33, 0xa000
	s_nop 0
	v_addc_co_u32_e64 v29, s[4:5], 0, v7, s[4:5]
	s_movk_i32 s4, 0x4000
	s_nop 0
	v_add_co_u32_e64 v30, s[4:5], s4, v6
	s_mov_b32 s6, 0xe000
	s_nop 0
	v_addc_co_u32_e64 v31, s[4:5], 0, v7, s[4:5]
	global_load_dwordx4 v[20:23], v[28:29], off sc0 sc1
	global_load_dwordx4 v[24:27], v[30:31], off sc0 sc1
	s_movk_i32 s4, 0x6000
	v_add_co_u32_e64 v40, s[4:5], s4, v6
	v_lshlrev_b32_e32 v57, 6, v1
	s_nop 0
	v_addc_co_u32_e64 v41, s[4:5], 0, v7, s[4:5]
	global_load_dwordx4 v[28:31], v[40:41], off sc0 sc1
	global_load_dwordx4 v[32:35], v[4:5], off offset:128 sc1 nt
	global_load_dwordx4 v[36:39], v[250:251], off offset:128 sc1 nt
	s_mov_b32 s4, 0x8000
	v_add_co_u32_e64 v40, s[4:5], s4, v6
	v_bitop3_b32 v58, v56, 48, v0 bitop3:0x48
	s_nop 0
	v_addc_co_u32_e64 v41, s[4:5], 0, v7, s[4:5]
	v_add_co_u32_e64 v44, s[4:5], s33, v6
	global_load_dwordx4 v[40:43], v[40:41], off sc0 sc1
	s_nop 0
	v_addc_co_u32_e64 v45, s[4:5], 0, v7, s[4:5]
	s_mov_b32 s4, 0xc000
	s_nop 0
	v_add_co_u32_e64 v48, s[4:5], s4, v6
	global_load_dwordx4 v[44:47], v[44:45], off sc0 sc1
	s_nop 0
	v_addc_co_u32_e64 v49, s[4:5], 0, v7, s[4:5]
	v_add_co_u32_e64 v52, s[4:5], s6, v6
	global_load_dwordx4 v[48:51], v[48:49], off sc0 sc1
	s_nop 0
	v_addc_co_u32_e64 v53, s[4:5], 0, v7, s[4:5]
	global_load_dwordx4 v[52:55], v[52:53], off sc0 sc1
	s_mov_b32 s4, 0x1e000
	v_bfe_u32 v57, v0, 1, 2
	v_bfe_u32 v58, v254, 2, 2
	v_xor_b32_e32 v57, v57, v58
	v_lshlrev_b32_e32 v57, 4, v57
	v_and_b32_e32 v58, 1, v0
	v_lshl_or_b32 v57, v58, 3, v57
	v_lshl_add_u32 v209, v254, 6, v57
	v_xor_b32_e32 v248, 32, v209
	v_add_u32_e32 v248, 0x200, v248
	v_add_u32_e32 v208, 0, v56
	v_readfirstlane_b32 s30, v0
	v_bfe_u32 v207, v0, 5, 1
	v_bitop3_b32 v1, v207, v1, 3 bitop3:0x78
	v_lshlrev_b32_e32 v210, 4, v1
	s_mov_b32 s34, 0x14000
	v_add_u32_e32 v213, 0x2000, v208
	s_mov_b32 s43, 0
	s_lshr_b32 s29, s30, 6
	s_mov_b32 s35, -2
	s_mov_b32 s36, 0xffff2000
	s_mov_b32 s37, 0xffff4000
	s_mov_b32 s38, 0xffff6000
	s_movk_i32 s39, 0x8000
	s_movk_i32 s40, 0xa000
	s_movk_i32 s41, 0xc000
	s_movk_i32 s42, 0xe000
	s_mov_b64 s[26:27], 0x100
	v_mov_b32_e32 v56, v3
	v_mov_b32_e32 v57, v3
	v_mov_b32_e32 v58, v3
	v_mov_b32_e32 v59, v3
	v_mov_b32_e32 v60, v3
	v_mov_b32_e32 v61, v3
	v_mov_b32_e32 v62, v3
	v_mov_b32_e32 v63, v3
	v_mov_b32_e32 v64, v3
	v_mov_b32_e32 v65, v3
	v_mov_b32_e32 v66, v3
	v_mov_b32_e32 v67, v3
	v_mov_b32_e32 v68, v3
	v_mov_b32_e32 v69, v3
	v_mov_b32_e32 v70, v3
	s_waitcnt vmcnt(11)
	v_cvt_pk_f16_f32 v8, v8, v9
	v_cvt_pk_f16_f32 v9, v10, v11
	s_waitcnt vmcnt(10)
	v_cvt_pk_f16_f32 v10, v12, v13
	v_cvt_pk_f16_f32 v11, v14, v15
	ds_write_b64 v209, v[8:9]
	ds_write_b64 v248, v[10:11]
	v_and_b32_e32 v10, 31, v0
	s_waitcnt vmcnt(9)
	ds_write_b128 v208, v[16:19] offset:8192
	s_waitcnt vmcnt(8)
	ds_write_b128 v208, v[20:23] offset:16384
	s_waitcnt vmcnt(7)
	ds_write_b128 v208, v[24:27] offset:24576
	s_load_dwordx2 s[16:17], s[0:1], 0x50
	s_load_dwordx4 s[12:15], s[0:1], 0x40
	s_load_dwordx8 s[4:11], s[0:1], 0x20
	s_lshl_b32 s0, s30, 1
	s_and_b32 s31, s0, 0x180
	s_lshr_b32 s0, s30, 2
	v_bfe_u32 v11, v0, 2, 2
	s_and_b32 s0, s0, 0x3fffffc0
	s_waitcnt vmcnt(5)
	v_cvt_pk_f16_f32 v8, v32, v33
	v_cvt_pk_f16_f32 v9, v34, v35
	v_or_b32_e32 v12, s31, v10
	v_or_b32_e32 v206, s0, v10
	v_bitop3_b32 v1, v207, v11, 2 bitop3:0x36
	s_waitcnt vmcnt(4)
	v_cvt_pk_f16_f32 v10, v36, v37
	v_cvt_pk_f16_f32 v11, v38, v39
	s_mov_b32 s0, 0x10000
	ds_write_b128 v208, v[28:31] offset:32768
	ds_write_b64 v209, v[8:9] offset:40960
	ds_write_b64 v248, v[10:11] offset:40960
	v_add_co_u32_e64 v8, s[0:1], s0, v6
	global_load_dwordx4 v[154:157], v[250:251], off offset:256 sc1 nt
	global_load_dwordx4 v[162:165], v[4:5], off offset:256 sc1 nt
	v_addc_co_u32_e64 v9, s[0:1], 0, v7, s[0:1]
	s_mov_b32 s0, 0x12000
	global_load_dwordx4 v[158:161], v[8:9], off sc0 sc1
	v_add_co_u32_e64 v8, s[0:1], s0, v6
	v_lshl_add_u32 v211, v12, 6, 0
	s_nop 0
	v_addc_co_u32_e64 v9, s[0:1], 0, v7, s[0:1]
	v_add_co_u32_e64 v10, s[0:1], s34, v6
	v_add_u32_e32 v14, 0x12000, v208
	s_nop 0
	v_addc_co_u32_e64 v11, s[0:1], 0, v7, s[0:1]
	s_mov_b32 s0, 0x16000
	s_nop 0
	v_add_co_u32_e64 v12, s[0:1], s0, v6
	s_waitcnt vmcnt(3)
	ds_write_b128 v14, v[52:55]
	v_addc_co_u32_e64 v13, s[0:1], 0, v7, s[0:1]
	s_mov_b32 s0, 0x18000
	s_nop 0
	v_add_co_u32_e64 v14, s[0:1], s0, v6
	ds_write_b128 v208, v[40:43] offset:49152
	s_nop 0
	v_addc_co_u32_e64 v15, s[0:1], 0, v7, s[0:1]
	s_mov_b32 s0, 0x1a000
	s_nop 0
	v_add_co_u32_e64 v16, s[0:1], s0, v6
	ds_write_b128 v208, v[44:47] offset:57344
	s_nop 0
	v_addc_co_u32_e64 v17, s[0:1], 0, v7, s[0:1]
	s_mov_b32 s0, 0x1c000
	ds_write_b128 v213, v[48:51] offset:57344
	v_add_co_u32_e64 v18, s[0:1], s0, v6
	v_add_u32_e32 v216, v211, v210
	s_nop 0
	v_addc_co_u32_e64 v19, s[0:1], 0, v7, s[0:1]
	global_load_dwordx4 v[174:177], v[8:9], off sc0 sc1
	global_load_dwordx4 v[166:169], v[10:11], off sc0 sc1
	global_load_dwordx4 v[170:173], v[12:13], off sc0 sc1
	global_load_dwordx4 v[142:145], v[250:251], off offset:384 sc1 nt
	global_load_dwordx4 v[150:153], v[4:5], off offset:384 sc1 nt
	global_load_dwordx4 v[138:141], v[14:15], off sc0 sc1
	global_load_dwordx4 v[146:149], v[16:17], off sc0 sc1
	global_load_dwordx4 v[134:137], v[18:19], off sc0 sc1
	s_mov_b32 s0, 0x1e000
	v_add_co_u32_e64 v8, s[0:1], s0, v6
	s_nop 1
	v_addc_co_u32_e64 v9, s[0:1], 0, v7, s[0:1]
	global_load_dwordx4 v[130:133], v[8:9], off sc0 sc1
	s_waitcnt lgkmcnt(0)
	s_barrier
	v_lshl_add_u32 v218, v206, 6, 0
	v_add_u32_e32 v217, v218, v210
	ds_read_b128 v[198:201], v216 offset:8192
	ds_read_b128 v[194:197], v216 offset:10240
	ds_read_b128 v[190:193], v216 offset:12288
	ds_read_b128 v[178:181], v216 offset:14336
	ds_read_b128 v[186:189], v217
	ds_read_b128 v[182:185], v217 offset:2048
	v_and_b32_e32 v20, 7, v0
	v_lshl_or_b32 v2, v20, 4, v2
	s_mov_b64 s[0:1], 0x2e000
	v_lshlrev_b32_e32 v212, 4, v1
	v_lshl_add_u64 v[202:203], v[6:7], 0, s[0:1]
	s_mov_b64 s[0:1], 0x290
	v_lshl_add_u64 v[4:5], s[24:25], 0, v[2:3]
	v_lshl_add_u64 v[204:205], v[4:5], 0, s[0:1]
	v_lshl_add_u64 v[252:253], v[204:205], 0, s[46:47]
	s_mov_b64 s[24:25], 0x10000
	v_mov_b32_e32 v2, v3
	v_mov_b32_e32 v4, v3
	v_mov_b32_e32 v5, v3
	v_mov_b32_e32 v6, v3
	v_mov_b32_e32 v7, v3
	v_mov_b32_e32 v8, v3
	v_mov_b32_e32 v9, v3
	v_mov_b32_e32 v10, v3
	v_mov_b32_e32 v11, v3
	v_mov_b32_e32 v12, v3
	v_mov_b32_e32 v13, v3
	v_mov_b32_e32 v14, v3
	v_mov_b32_e32 v15, v3
	v_mov_b32_e32 v16, v3
	v_mov_b32_e32 v17, v3
	v_mov_b32_e32 v18, v3
	v_mov_b32_e32 v19, v3
	v_mov_b32_e32 v20, v3
	v_mov_b32_e32 v21, v3
	v_mov_b32_e32 v22, v3
	v_mov_b32_e32 v23, v3
	v_mov_b32_e32 v24, v3
	v_mov_b32_e32 v25, v3
	v_mov_b32_e32 v26, v3
	v_mov_b32_e32 v27, v3
	v_mov_b32_e32 v28, v3
	v_mov_b32_e32 v29, v3
	v_mov_b32_e32 v30, v3
	v_mov_b32_e32 v31, v3
	v_mov_b32_e32 v32, v3
	v_mov_b32_e32 v33, v3
	v_mov_b32_e32 v34, v3
	v_mov_b32_e32 v35, v3
	v_mov_b32_e32 v36, v3
	v_mov_b32_e32 v37, v3
	v_mov_b32_e32 v38, v3
	v_mov_b32_e32 v39, v3
	v_mov_b32_e32 v40, v3
	v_mov_b32_e32 v41, v3
	v_mov_b32_e32 v42, v3
	v_mov_b32_e32 v43, v3
	v_mov_b32_e32 v44, v3
	v_mov_b32_e32 v45, v3
	v_mov_b32_e32 v46, v3
	v_mov_b32_e32 v47, v3
	v_mov_b32_e32 v48, v3
	v_mov_b32_e32 v49, v3
	v_mov_b32_e32 v50, v3
	v_mov_b32_e32 v51, v3
	v_mov_b32_e32 v52, v3
	v_mov_b32_e32 v53, v3
	v_mov_b32_e32 v54, v3
	v_mov_b32_e32 v55, v3
	v_mov_b32_e32 v71, v3
	v_mov_b32_e32 v72, v3
	v_mov_b32_e32 v73, v3
	v_mov_b32_e32 v74, v3
	v_mov_b32_e32 v75, v3
	v_mov_b32_e32 v76, v3
	v_mov_b32_e32 v77, v3
	v_mov_b32_e32 v78, v3
	v_mov_b32_e32 v79, v3
	v_mov_b32_e32 v80, v3
	v_mov_b32_e32 v81, v3
	v_mov_b32_e32 v82, v3
	v_mov_b32_e32 v83, v3
	v_mov_b32_e32 v84, v3
	v_mov_b32_e32 v85, v3
	v_mov_b32_e32 v86, v3
	v_mov_b32_e32 v87, v3
	v_mov_b32_e32 v88, v3
	v_mov_b32_e32 v89, v3
	v_mov_b32_e32 v90, v3
	v_mov_b32_e32 v91, v3
	v_mov_b32_e32 v92, v3
	v_mov_b32_e32 v93, v3
	v_mov_b32_e32 v94, v3
	v_mov_b32_e32 v95, v3
	v_mov_b32_e32 v96, v3
	v_mov_b32_e32 v97, v3
	v_mov_b32_e32 v98, v3
	v_mov_b32_e32 v99, v3
	v_mov_b32_e32 v100, v3
	v_mov_b32_e32 v101, v3
	v_mov_b32_e32 v102, v3
	v_mov_b32_e32 v103, v3
	v_mov_b32_e32 v104, v3
	v_mov_b32_e32 v105, v3
	v_mov_b32_e32 v106, v3
	v_mov_b32_e32 v107, v3
	v_mov_b32_e32 v108, v3
	v_mov_b32_e32 v109, v3
	v_mov_b32_e32 v110, v3
	v_mov_b32_e32 v111, v3
	v_mov_b32_e32 v112, v3
	v_mov_b32_e32 v113, v3
	v_mov_b32_e32 v114, v3
	v_mov_b32_e32 v115, v3
	v_mov_b32_e32 v116, v3
	v_mov_b32_e32 v117, v3
	v_mov_b32_e32 v118, v3
	v_mov_b32_e32 v119, v3
	v_mov_b32_e32 v120, v3
	v_mov_b32_e32 v121, v3
	v_mov_b32_e32 v122, v3
	v_mov_b32_e32 v123, v3
	v_mov_b32_e32 v124, v3
	v_mov_b32_e32 v125, v3
	v_mov_b32_e32 v126, v3
	v_mov_b32_e32 v127, v3
	v_mov_b32_e32 v128, v3
	v_mov_b32_e32 v129, v3
	v_and_b32_e32 v1, 63, v0
	v_add_u32_e32 v215, v211, v212
	v_add_u32_e32 v214, v218, v212
.LBB1_1:
	s_waitcnt lgkmcnt(0)
	v_mfma_f32_32x32x16_f16 v[114:129], v[198:201], v[186:189], v[114:129]
	s_mov_b32 s44, s33
	s_mov_b32 s33, s43
	v_mfma_f32_32x32x16_f16 v[98:113], v[198:201], v[182:185], v[98:113]
	v_add_u32_e32 v219, s33, v215
	ds_read_b128 v[198:201], v219 offset:8192
	ds_read_b128 v[220:223], v219 offset:10240
	ds_read_b128 v[224:227], v219 offset:12288
	ds_read_b128 v[228:231], v219 offset:14336
	v_add_u32_e32 v219, s33, v214
	ds_read_b128 v[232:235], v219
	ds_read_b128 v[236:239], v219 offset:2048
	s_waitcnt vmcnt(10)
	v_cvt_pk_f16_f32 v162, v162, v163
	v_cvt_pk_f16_f32 v163, v164, v165
	v_cvt_pk_f16_f32 v164, v154, v155
	v_cvt_pk_f16_f32 v165, v156, v157
	v_add_u32_e32 v154, s34, v209
	ds_write_b64 v154, v[162:163]
	v_add_u32_e32 v154, s34, v248
	ds_write_b64 v154, v[164:165]
	v_mfma_f32_32x32x16_f16 v[82:97], v[194:197], v[186:189], v[82:97]
	v_add_u32_e32 v154, s34, v208
	s_waitcnt vmcnt(9)
	ds_write_b128 v154, v[158:161] offset:8192
	s_waitcnt vmcnt(8)
	ds_write_b128 v154, v[174:177] offset:16384
	v_mfma_f32_32x32x16_f16 v[66:81], v[194:197], v[182:185], v[66:81]
	v_mfma_f32_32x32x16_f16 v[50:65], v[190:193], v[186:189], v[50:65]
	s_waitcnt vmcnt(7)
	ds_write_b128 v154, v[166:169] offset:24576
	s_waitcnt vmcnt(6)
	ds_write_b128 v154, v[170:173] offset:32768
	v_mfma_f32_32x32x16_f16 v[34:49], v[190:193], v[182:185], v[34:49]
	v_add_co_u32_e64 v158, s[0:1], s36, v202
	global_load_dwordx4 v[154:157], v[252:253], off offset:-144 sc1 nt
	global_load_dwordx4 v[162:165], v[204:205], off offset:-144 sc1 nt
	v_addc_co_u32_e64 v159, s[0:1], -1, v203, s[0:1]
	v_add_co_u32_e64 v166, s[0:1], s37, v202
	v_mfma_f32_32x32x16_f16 v[18:33], v[178:181], v[186:189], v[18:33]
	s_nop 0
	v_addc_co_u32_e64 v167, s[0:1], -1, v203, s[0:1]
	global_load_dwordx4 v[158:161], v[158:159], off sc0 sc1
	s_nop 0
	global_load_dwordx4 v[174:177], v[166:167], off sc0 sc1
	v_add_co_u32_e64 v166, s[0:1], s38, v202
	s_nop 1
	v_addc_co_u32_e64 v167, s[0:1], -1, v203, s[0:1]
	v_add_co_u32_e64 v170, s[0:1], s39, v202
	v_mfma_f32_32x32x16_f16 v[2:17], v[178:181], v[182:185], v[2:17]
	s_nop 0
	v_addc_co_u32_e64 v171, s[0:1], -1, v203, s[0:1]
	global_load_dwordx4 v[166:169], v[166:167], off sc0 sc1
	s_nop 0
	global_load_dwordx4 v[170:173], v[170:171], off sc0 sc1
	v_add_u32_e32 v190, s44, v216
	ds_read_b128 v[178:181], v190 offset:8192
	ds_read_b128 v[182:185], v190 offset:10240
	ds_read_b128 v[186:189], v190 offset:12288
	ds_read_b128 v[190:193], v190 offset:14336
	v_add_u32_e32 v219, s44, v217
	ds_read_b128 v[194:197], v219
	ds_read_b128 v[240:243], v219 offset:2048
	s_waitcnt lgkmcnt(12)
	v_mfma_f32_32x32x16_f16 v[114:129], v[198:201], v[232:235], v[114:129]
	s_waitcnt lgkmcnt(11)
	v_mfma_f32_32x32x16_f16 v[98:113], v[198:201], v[236:239], v[98:113]
	v_mfma_f32_32x32x16_f16 v[82:97], v[220:223], v[232:235], v[82:97]
	v_mfma_f32_32x32x16_f16 v[66:81], v[220:223], v[236:239], v[66:81]
	v_mfma_f32_32x32x16_f16 v[50:65], v[224:227], v[232:235], v[50:65]
	v_mfma_f32_32x32x16_f16 v[34:49], v[224:227], v[236:239], v[34:49]
	v_mfma_f32_32x32x16_f16 v[18:33], v[228:231], v[232:235], v[18:33]
	v_mfma_f32_32x32x16_f16 v[2:17], v[228:231], v[236:239], v[2:17]
	s_waitcnt lgkmcnt(1)
	v_mfma_f32_32x32x16_f16 v[114:129], v[178:181], v[194:197], v[114:129]
	s_waitcnt lgkmcnt(0)
	s_barrier
	s_waitcnt lgkmcnt(0)
	v_mfma_f32_32x32x16_f16 v[98:113], v[178:181], v[240:243], v[98:113]
	v_add_u32_e32 v178, s44, v215
	ds_read_b128 v[220:223], v178 offset:8192
	ds_read_b128 v[224:227], v178 offset:10240
	ds_read_b128 v[228:231], v178 offset:12288
	ds_read_b128 v[232:235], v178 offset:14336
	v_add_u32_e32 v178, s44, v214
	ds_read_b128 v[236:239], v178
	ds_read_b128 v[244:247], v178 offset:2048
	s_waitcnt vmcnt(10)
	v_cvt_pk_f16_f32 v150, v150, v151
	v_cvt_pk_f16_f32 v151, v152, v153
	v_cvt_pk_f16_f32 v152, v142, v143
	v_cvt_pk_f16_f32 v153, v144, v145
	v_add_u32_e32 v142, s33, v209
	ds_write_b64 v142, v[150:151]
	v_add_u32_e32 v142, s33, v248
	ds_write_b64 v142, v[152:153]
	v_mfma_f32_32x32x16_f16 v[82:97], v[182:185], v[194:197], v[82:97]
	v_add_u32_e32 v142, s33, v208
	s_waitcnt vmcnt(9)
	ds_write_b128 v142, v[138:141] offset:8192
	s_waitcnt vmcnt(8)
	ds_write_b128 v142, v[146:149] offset:16384
	v_mfma_f32_32x32x16_f16 v[66:81], v[182:185], v[240:243], v[66:81]
	v_mfma_f32_32x32x16_f16 v[50:65], v[186:189], v[194:197], v[50:65]
	s_waitcnt vmcnt(7)
	ds_write_b128 v142, v[134:137] offset:24576
	s_waitcnt vmcnt(6)
	ds_write_b128 v142, v[130:133] offset:32768
	v_mfma_f32_32x32x16_f16 v[34:49], v[186:189], v[240:243], v[34:49]
	v_add_co_u32_e64 v130, s[0:1], s40, v202
	global_load_dwordx4 v[142:145], v[252:253], off offset:-16 sc1 nt
	global_load_dwordx4 v[150:153], v[204:205], off offset:-16 sc1 nt
	v_addc_co_u32_e64 v131, s[0:1], -1, v203, s[0:1]
	v_add_co_u32_e64 v132, s[0:1], s41, v202
	v_mfma_f32_32x32x16_f16 v[18:33], v[190:193], v[194:197], v[18:33]
	s_nop 0
	v_addc_co_u32_e64 v133, s[0:1], -1, v203, s[0:1]
	global_load_dwordx4 v[138:141], v[130:131], off sc0 sc1
	global_load_dwordx4 v[146:149], v[132:133], off sc0 sc1
	v_add_co_u32_e64 v130, s[0:1], s42, v202
	s_nop 1
	v_addc_co_u32_e64 v131, s[0:1], -1, v203, s[0:1]
	global_load_dwordx4 v[134:137], v[130:131], off sc0 sc1
	s_nop 0
	global_load_dwordx4 v[130:133], v[202:203], off sc0 sc1
	v_mfma_f32_32x32x16_f16 v[2:17], v[190:193], v[240:243], v[2:17]
	v_add_u32_e32 v178, s34, v216
	ds_read_b128 v[198:201], v178 offset:8192
	ds_read_b128 v[194:197], v178 offset:10240
	ds_read_b128 v[190:193], v178 offset:12288
	ds_read_b128 v[178:181], v178 offset:14336
	v_add_u32_e32 v182, s34, v217
	ds_read_b128 v[186:189], v182
	ds_read_b128 v[182:185], v182 offset:2048
	s_waitcnt lgkmcnt(12)
	v_mfma_f32_32x32x16_f16 v[114:129], v[220:223], v[236:239], v[114:129]
	s_waitcnt lgkmcnt(11)
	v_mfma_f32_32x32x16_f16 v[98:113], v[220:223], v[244:247], v[98:113]
	v_mfma_f32_32x32x16_f16 v[82:97], v[224:227], v[236:239], v[82:97]
	v_mfma_f32_32x32x16_f16 v[66:81], v[224:227], v[244:247], v[66:81]
	v_mfma_f32_32x32x16_f16 v[50:65], v[228:231], v[236:239], v[50:65]
	v_mfma_f32_32x32x16_f16 v[34:49], v[228:231], v[244:247], v[34:49]
	v_mfma_f32_32x32x16_f16 v[18:33], v[232:235], v[236:239], v[18:33]
	v_mfma_f32_32x32x16_f16 v[2:17], v[232:235], v[244:247], v[2:17]
	s_waitcnt lgkmcnt(0)
	s_barrier
	s_add_i32 s35, s35, 2
	v_lshl_add_u64 v[202:203], v[202:203], 0, s[24:25]
	v_lshl_add_u64 v[204:205], v[204:205], 0, s[26:27]
	v_lshl_add_u64 v[252:253], v[252:253], 0, s[26:27]
	s_mov_b32 s43, s34
	s_cmp_gt_u32 s35, 9
	s_mov_b32 s34, s44
	s_cbranch_scc0 .LBB1_1
	s_and_b64 s[0:1], s[20:21], exec
	s_cselect_b32 s6, s6, s8
	s_cselect_b32 s7, s7, s9
	s_and_b64 s[0:1], vcc, exec
	s_cselect_b32 s1, s5, s7
	s_cselect_b32 s0, s4, s6
	v_mov_b32_e32 v202, 0x3e38aa3b
	s_waitcnt lgkmcnt(1)
	v_mfma_f32_32x32x16_f16 v[114:129], v[198:201], v[186:189], v[114:129]
	v_cndmask_b32_e32 v202, 1.0, v202, vcc
	s_waitcnt lgkmcnt(0)
	v_mfma_f32_32x32x16_f16 v[98:113], v[198:201], v[182:185], v[98:113]
	ds_read_b128 v[198:201], v215 offset:8192
	ds_read_b128 v[220:223], v215 offset:10240
	ds_read_b128 v[224:227], v215 offset:12288
	ds_read_b128 v[228:231], v215 offset:14336
	ds_read_b128 v[232:235], v214
	ds_read_b128 v[236:239], v214 offset:2048
	s_waitcnt vmcnt(10)
	v_cvt_pk_f16_f32 v162, v162, v163
	v_cvt_pk_f16_f32 v163, v164, v165
	v_cvt_pk_f16_f32 v164, v154, v155
	v_cvt_pk_f16_f32 v165, v156, v157
	v_add_u32_e32 v154, 0x14000, v209
	ds_write_b64 v154, v[162:163]
	v_add_u32_e32 v154, 0x14000, v248
	ds_write_b64 v154, v[164:165]
	v_add_u32_e32 v154, 0x14000, v213
	s_waitcnt vmcnt(9)
	ds_write_b128 v154, v[158:161]
	v_add_u32_e32 v154, 0x16000, v213
	v_mfma_f32_32x32x16_f16 v[82:97], v[194:197], v[186:189], v[82:97]
	s_waitcnt vmcnt(8)
	ds_write_b128 v154, v[174:177]
	v_mfma_f32_32x32x16_f16 v[66:81], v[194:197], v[182:185], v[66:81]
	v_add_u32_e32 v154, 0x18000, v213
	s_waitcnt vmcnt(7)
	ds_write_b128 v154, v[166:169]
	v_add_u32_e32 v154, 0x1a000, v213
	v_mfma_f32_32x32x16_f16 v[50:65], v[190:193], v[186:189], v[50:65]
	s_waitcnt vmcnt(6)
	ds_write_b128 v154, v[170:173]
	v_mfma_f32_32x32x16_f16 v[34:49], v[190:193], v[182:185], v[34:49]
	v_mfma_f32_32x32x16_f16 v[18:33], v[178:181], v[186:189], v[18:33]
	v_mfma_f32_32x32x16_f16 v[2:17], v[178:181], v[182:185], v[2:17]
	ds_read_b128 v[154:157], v216 offset:49152
	ds_read_b128 v[158:161], v216 offset:51200
	ds_read_b128 v[162:165], v216 offset:53248
	ds_read_b128 v[166:169], v216 offset:55296
	ds_read_b128 v[170:173], v217 offset:40960
	ds_read_b128 v[174:177], v217 offset:43008
	s_waitcnt lgkmcnt(12)
	v_mfma_f32_32x32x16_f16 v[114:129], v[198:201], v[232:235], v[114:129]
	s_waitcnt lgkmcnt(11)
	v_mfma_f32_32x32x16_f16 v[98:113], v[198:201], v[236:239], v[98:113]
	v_mfma_f32_32x32x16_f16 v[82:97], v[220:223], v[232:235], v[82:97]
	v_mfma_f32_32x32x16_f16 v[66:81], v[220:223], v[236:239], v[66:81]
	v_mfma_f32_32x32x16_f16 v[50:65], v[224:227], v[232:235], v[50:65]
	v_mfma_f32_32x32x16_f16 v[34:49], v[224:227], v[236:239], v[34:49]
	v_mfma_f32_32x32x16_f16 v[18:33], v[228:231], v[232:235], v[18:33]
	v_mfma_f32_32x32x16_f16 v[2:17], v[228:231], v[236:239], v[2:17]
	s_waitcnt lgkmcnt(0)
	s_barrier
	s_waitcnt lgkmcnt(1)
	v_mfma_f32_32x32x16_f16 v[114:129], v[154:157], v[170:173], v[114:129]
	s_waitcnt lgkmcnt(0)
	v_mfma_f32_32x32x16_f16 v[98:113], v[154:157], v[174:177], v[98:113]
	ds_read_b128 v[154:157], v215 offset:49152
	ds_read_b128 v[178:181], v215 offset:51200
	ds_read_b128 v[182:185], v215 offset:53248
	ds_read_b128 v[186:189], v215 offset:55296
	ds_read_b128 v[190:193], v214 offset:40960
	ds_read_b128 v[194:197], v214 offset:43008
	s_waitcnt vmcnt(4)
	v_cvt_pk_f16_f32 v150, v150, v151
	v_cvt_pk_f16_f32 v151, v152, v153
	v_cvt_pk_f16_f32 v152, v142, v143
	v_cvt_pk_f16_f32 v153, v144, v145
	ds_write_b64 v209, v[150:151]
	ds_write_b64 v248, v[152:153]
	v_mfma_f32_32x32x16_f16 v[82:97], v[158:161], v[170:173], v[82:97]
	s_waitcnt vmcnt(3)
	ds_write_b128 v208, v[138:141] offset:8192
	s_waitcnt vmcnt(2)
	ds_write_b128 v208, v[146:149] offset:16384
	v_mfma_f32_32x32x16_f16 v[66:81], v[158:161], v[174:177], v[66:81]
	v_mfma_f32_32x32x16_f16 v[50:65], v[162:165], v[170:173], v[50:65]
	s_waitcnt vmcnt(1)
	ds_write_b128 v208, v[134:137] offset:24576
	s_waitcnt vmcnt(0)
	ds_write_b128 v208, v[130:133] offset:32768
	v_mfma_f32_32x32x16_f16 v[34:49], v[162:165], v[174:177], v[34:49]
	v_mfma_f32_32x32x16_f16 v[18:33], v[166:169], v[170:173], v[18:33]
	v_mfma_f32_32x32x16_f16 v[2:17], v[166:169], v[174:177], v[2:17]
	v_add_u32_e32 v158, 0x16000, v211
	v_add_u32_e32 v142, v158, v210
	ds_read_b128 v[130:133], v142
	ds_read_b128 v[134:137], v142 offset:2048
	ds_read_b128 v[138:141], v142 offset:4096
	ds_read_b128 v[142:145], v142 offset:6144
	v_add_u32_e32 v166, 0x14000, v218
	v_add_u32_e32 v150, v166, v210
	ds_read_b128 v[146:149], v150
	ds_read_b128 v[150:153], v150 offset:2048
	s_waitcnt lgkmcnt(12)
	v_mfma_f32_32x32x16_f16 v[114:129], v[154:157], v[190:193], v[114:129]
	s_waitcnt lgkmcnt(11)
	v_mfma_f32_32x32x16_f16 v[98:113], v[154:157], v[194:197], v[98:113]
	v_mfma_f32_32x32x16_f16 v[82:97], v[178:181], v[190:193], v[82:97]
	v_mfma_f32_32x32x16_f16 v[66:81], v[178:181], v[194:197], v[66:81]
	v_mfma_f32_32x32x16_f16 v[50:65], v[182:185], v[190:193], v[50:65]
	v_mfma_f32_32x32x16_f16 v[34:49], v[182:185], v[194:197], v[34:49]
	v_mfma_f32_32x32x16_f16 v[18:33], v[186:189], v[190:193], v[18:33]
	v_mfma_f32_32x32x16_f16 v[2:17], v[186:189], v[194:197], v[2:17]
	s_waitcnt lgkmcnt(0)
	s_barrier
	s_waitcnt lgkmcnt(1)
	v_mfma_f32_32x32x16_f16 v[114:129], v[130:133], v[146:149], v[114:129]
	s_waitcnt lgkmcnt(0)
	v_mfma_f32_32x32x16_f16 v[98:113], v[130:133], v[150:153], v[98:113]
	v_add_u32_e32 v162, v158, v212
	ds_read_b128 v[130:133], v162
	ds_read_b128 v[154:157], v162 offset:2048
	ds_read_b128 v[158:161], v162 offset:4096
	ds_read_b128 v[162:165], v162 offset:6144
	v_add_u32_e32 v170, v166, v212
	ds_read_b128 v[166:169], v170
	ds_read_b128 v[170:173], v170 offset:2048
	v_mfma_f32_32x32x16_f16 v[82:97], v[134:137], v[146:149], v[82:97]
	v_mfma_f32_32x32x16_f16 v[66:81], v[134:137], v[150:153], v[66:81]
	v_mfma_f32_32x32x16_f16 v[50:65], v[138:141], v[146:149], v[50:65]
	v_mfma_f32_32x32x16_f16 v[34:49], v[138:141], v[150:153], v[34:49]
	v_mfma_f32_32x32x16_f16 v[18:33], v[142:145], v[146:149], v[18:33]
	v_mfma_f32_32x32x16_f16 v[2:17], v[142:145], v[150:153], v[2:17]
	ds_read_b128 v[134:137], v216 offset:8192
	ds_read_b128 v[138:141], v216 offset:10240
	ds_read_b128 v[142:145], v216 offset:12288
	ds_read_b128 v[146:149], v216 offset:14336
	ds_read_b128 v[150:153], v217
	ds_read_b128 v[174:177], v217 offset:2048
	s_waitcnt lgkmcnt(7)
	v_mfma_f32_32x32x16_f16 v[114:129], v[130:133], v[166:169], v[114:129]
	s_waitcnt lgkmcnt(6)
	v_mfma_f32_32x32x16_f16 v[98:113], v[130:133], v[170:173], v[98:113]
	v_mfma_f32_32x32x16_f16 v[82:97], v[154:157], v[166:169], v[82:97]
	v_mfma_f32_32x32x16_f16 v[66:81], v[154:157], v[170:173], v[66:81]
	v_mfma_f32_32x32x16_f16 v[50:65], v[158:161], v[166:169], v[50:65]
	v_mfma_f32_32x32x16_f16 v[34:49], v[158:161], v[170:173], v[34:49]
	v_mfma_f32_32x32x16_f16 v[18:33], v[162:165], v[166:169], v[18:33]
	v_mfma_f32_32x32x16_f16 v[2:17], v[162:165], v[170:173], v[2:17]
	s_waitcnt lgkmcnt(0)
	s_barrier
	s_waitcnt lgkmcnt(1)
	v_mfma_f32_32x32x16_f16 v[114:129], v[134:137], v[150:153], v[114:129]
	s_waitcnt lgkmcnt(0)
	v_mfma_f32_32x32x16_f16 v[98:113], v[134:137], v[174:177], v[98:113]
	ds_read_b128 v[130:133], v215 offset:8192
	ds_read_b128 v[134:137], v215 offset:10240
	ds_read_b128 v[154:157], v215 offset:12288
	ds_read_b128 v[158:161], v215 offset:14336
	ds_read_b128 v[162:165], v214
	ds_read_b128 v[166:169], v214 offset:2048
	v_mfma_f32_32x32x16_f16 v[82:97], v[138:141], v[150:153], v[82:97]
	v_mfma_f32_32x32x16_f16 v[66:81], v[138:141], v[174:177], v[66:81]
	v_mfma_f32_32x32x16_f16 v[50:65], v[142:145], v[150:153], v[50:65]
	v_mfma_f32_32x32x16_f16 v[34:49], v[142:145], v[174:177], v[34:49]
	v_mfma_f32_32x32x16_f16 v[18:33], v[146:149], v[150:153], v[18:33]
	v_mfma_f32_32x32x16_f16 v[2:17], v[146:149], v[174:177], v[2:17]
	s_waitcnt lgkmcnt(1)
	v_mfma_f32_32x32x16_f16 v[114:129], v[130:133], v[162:165], v[114:129]
	s_waitcnt lgkmcnt(0)
	v_mfma_f32_32x32x16_f16 v[98:113], v[130:133], v[166:169], v[98:113]
	v_mfma_f32_32x32x16_f16 v[82:97], v[134:137], v[162:165], v[82:97]
	v_mfma_f32_32x32x16_f16 v[66:81], v[134:137], v[166:169], v[66:81]
	v_mfma_f32_32x32x16_f16 v[50:65], v[154:157], v[162:165], v[50:65]
	v_mfma_f32_32x32x16_f16 v[34:49], v[154:157], v[166:169], v[34:49]
	v_mfma_f32_32x32x16_f16 v[18:33], v[158:161], v[162:165], v[18:33]
	v_mfma_f32_32x32x16_f16 v[2:17], v[158:161], v[166:169], v[2:17]
	v_lshl_or_b32 v130, v207, 2, s31
	s_waitcnt lgkmcnt(0)
	s_barrier
	s_cbranch_vccnz .Lepi_q
	v_lshlrev_b32_e32 v154, 2, v130
	global_load_dwordx4 v[134:137], v154, s[0:1]
	global_load_dwordx4 v[150:153], v154, s[0:1] offset:32
	global_load_dwordx4 v[156:159], v154, s[0:1] offset:64
	global_load_dwordx4 v[160:163], v154, s[0:1] offset:96
	global_load_dwordx4 v[164:167], v154, s[0:1] offset:128
	global_load_dwordx4 v[168:171], v154, s[0:1] offset:160
	s_movk_i32 s4, 0x410
	v_lshlrev_b32_e32 v130, 1, v130
	v_mul_lo_u32 v131, v206, s4
	v_add3_u32 v155, 0, v130, v131
	global_load_dwordx4 v[172:175], v154, s[0:1] offset:192
	global_load_dwordx4 v[146:149], v154, s[0:1] offset:224
	global_load_dwordx4 v[142:145], v154, s[0:1] offset:256
	global_load_dwordx4 v[130:133], v154, s[0:1] offset:288
	global_load_dwordx4 v[138:141], v154, s[0:1] offset:320
	v_add_u32_e32 v176, 0x8000, v155
	s_waitcnt vmcnt(10)
	v_pk_add_f32 v[114:115], v[134:135], v[114:115]
	v_pk_add_f32 v[116:117], v[136:137], v[116:117]
	v_pk_add_f32 v[98:99], v[134:135], v[98:99]
	v_pk_add_f32 v[100:101], v[136:137], v[100:101]
	s_waitcnt vmcnt(9)
	v_pk_add_f32 v[118:119], v[150:151], v[118:119]
	v_pk_add_f32 v[120:121], v[152:153], v[120:121]
	s_waitcnt vmcnt(6)
	v_pk_add_f32 v[82:83], v[164:165], v[82:83]
	v_pk_add_f32 v[84:85], v[166:167], v[84:85]
	v_pk_add_f32 v[66:67], v[164:165], v[66:67]
	v_pk_add_f32 v[68:69], v[166:167], v[68:69]
	s_waitcnt vmcnt(5)
	v_pk_add_f32 v[70:71], v[168:169], v[70:71]
	v_pk_add_f32 v[72:73], v[170:171], v[72:73]
	v_pk_add_f32 v[102:103], v[150:151], v[102:103]
	v_pk_add_f32 v[104:105], v[152:153], v[104:105]
	v_pk_add_f32 v[122:123], v[156:157], v[122:123]
	v_pk_add_f32 v[124:125], v[158:159], v[124:125]
	v_pk_add_f32 v[106:107], v[156:157], v[106:107]
	v_pk_add_f32 v[108:109], v[158:159], v[108:109]
	v_pk_add_f32 v[126:127], v[160:161], v[126:127]
	v_pk_add_f32 v[128:129], v[162:163], v[128:129]
	v_pk_add_f32 v[110:111], v[160:161], v[110:111]
	v_pk_add_f32 v[112:113], v[162:163], v[112:113]
	v_pk_add_f32 v[86:87], v[168:169], v[86:87]
	v_pk_add_f32 v[88:89], v[170:171], v[88:89]
	v_cvt_pk_f16_f32 v114, v114, v115
	v_cvt_pk_f16_f32 v115, v116, v117
	v_cvt_pk_f16_f32 v98, v98, v99
	v_cvt_pk_f16_f32 v99, v100, v101
	v_cvt_pk_f16_f32 v100, v118, v119
	v_cvt_pk_f16_f32 v101, v120, v121
	v_cvt_pk_f16_f32 v82, v82, v83
	v_cvt_pk_f16_f32 v83, v84, v85
	v_cvt_pk_f16_f32 v84, v66, v67
	v_cvt_pk_f16_f32 v85, v68, v69
	v_cvt_pk_f16_f32 v70, v70, v71
	v_cvt_pk_f16_f32 v71, v72, v73
	v_cvt_pk_f16_f32 v102, v102, v103
	v_cvt_pk_f16_f32 v103, v104, v105
	v_cvt_pk_f16_f32 v104, v122, v123
	v_cvt_pk_f16_f32 v105, v124, v125
	v_cvt_pk_f16_f32 v106, v106, v107
	v_cvt_pk_f16_f32 v107, v108, v109
	v_cvt_pk_f16_f32 v108, v126, v127
	v_cvt_pk_f16_f32 v109, v128, v129
	v_cvt_pk_f16_f32 v110, v110, v111
	v_cvt_pk_f16_f32 v111, v112, v113
	v_cvt_pk_f16_f32 v86, v86, v87
	ds_write2_b64 v155, v[114:115], v[100:101] offset1:2
	ds_write2_b64 v176, v[98:99], v[102:103] offset0:64 offset1:66
	ds_write2_b64 v155, v[104:105], v[108:109] offset0:4 offset1:6
	ds_write2_b64 v176, v[106:107], v[110:111] offset0:68 offset1:70
	v_cvt_pk_f16_f32 v87, v88, v89
	ds_write2_b64 v176, v[84:85], v[70:71] offset0:72 offset1:74
	s_waitcnt vmcnt(4)
	v_pk_add_f32 v[70:71], v[172:173], v[90:91]
	v_pk_add_f32 v[84:85], v[174:175], v[92:93]
	v_pk_add_f32 v[74:75], v[172:173], v[74:75]
	ds_write2_b64 v155, v[82:83], v[86:87] offset0:8 offset1:10
	v_mov_b64_e32 v[82:83], v[70:71]
	global_load_dwordx4 v[66:69], v154, s[0:1] offset:352
	global_load_dwordx4 v[70:73], v154, s[0:1] offset:384
	v_cvt_pk_f16_f32 v82, v82, v83
	v_cvt_pk_f16_f32 v83, v84, v85
	v_cvt_pk_f16_f32 v84, v74, v75
	v_pk_add_f32 v[74:75], v[174:175], v[76:77]
	s_waitcnt vmcnt(5)
	v_pk_add_f32 v[78:79], v[146:147], v[78:79]
	v_cvt_pk_f16_f32 v85, v74, v75
	global_load_dwordx4 v[74:77], v154, s[0:1] offset:416
	v_pk_add_f32 v[80:81], v[148:149], v[80:81]
	v_cvt_pk_f16_f32 v78, v78, v79
	v_cvt_pk_f16_f32 v79, v80, v81
	ds_write2_b64 v176, v[84:85], v[78:79] offset0:76 offset1:78
	global_load_dwordx4 v[78:81], v154, s[0:1] offset:448
	v_pk_add_f32 v[86:87], v[146:147], v[94:95]
	v_pk_add_f32 v[88:89], v[148:149], v[96:97]
	s_waitcnt vmcnt(6)
	v_pk_add_f32 v[50:51], v[142:143], v[50:51]
	v_pk_add_f32 v[52:53], v[144:145], v[52:53]
	v_pk_add_f32 v[34:35], v[142:143], v[34:35]
	v_cvt_pk_f16_f32 v86, v86, v87
	v_cvt_pk_f16_f32 v87, v88, v89
	v_cvt_pk_f16_f32 v50, v50, v51
	v_cvt_pk_f16_f32 v51, v52, v53
	v_cvt_pk_f16_f32 v52, v34, v35
	v_pk_add_f32 v[34:35], v[144:145], v[36:37]
	ds_write2_b64 v155, v[82:83], v[86:87] offset0:12 offset1:14
	v_mov_b64_e32 v[82:83], v[34:35]
	global_load_dwordx4 v[34:37], v154, s[0:1] offset:480
	s_waitcnt vmcnt(6)
	v_pk_add_f32 v[38:39], v[130:131], v[38:39]
	v_pk_add_f32 v[40:41], v[132:133], v[40:41]
	v_cvt_pk_f16_f32 v53, v82, v83
	v_cvt_pk_f16_f32 v38, v38, v39
	v_cvt_pk_f16_f32 v39, v40, v41
	ds_write2_b64 v176, v[52:53], v[38:39] offset0:80 offset1:82
	s_waitcnt vmcnt(5)
	v_pk_add_f32 v[38:39], v[138:139], v[58:59]
	v_pk_add_f32 v[40:41], v[140:141], v[60:61]
	v_cvt_pk_f16_f32 v38, v38, v39
	v_cvt_pk_f16_f32 v39, v40, v41
	v_pk_add_f32 v[40:41], v[138:139], v[42:43]
	v_pk_add_f32 v[42:43], v[140:141], v[44:45]
	v_cvt_pk_f16_f32 v40, v40, v41
	v_cvt_pk_f16_f32 v41, v42, v43
	v_pk_add_f32 v[54:55], v[130:131], v[54:55]
	v_pk_add_f32 v[56:57], v[132:133], v[56:57]
	v_cmp_gt_u32_e64 s[0:1], 8, v0
	v_cvt_pk_f16_f32 v54, v54, v55
	v_cvt_pk_f16_f32 v55, v56, v57
	s_and_b64 s[6:7], s[20:21], s[0:1]
	ds_write2_b64 v155, v[50:51], v[54:55] offset0:16 offset1:18
	s_waitcnt vmcnt(4)
	v_pk_add_f32 v[42:43], v[66:67], v[62:63]
	s_waitcnt vmcnt(3)
	v_pk_add_f32 v[18:19], v[70:71], v[18:19]
	v_pk_add_f32 v[20:21], v[72:73], v[20:21]
	v_pk_add_f32 v[2:3], v[70:71], v[2:3]
	v_pk_add_f32 v[4:5], v[72:73], v[4:5]
	v_cvt_pk_f16_f32 v18, v18, v19
	v_cvt_pk_f16_f32 v19, v20, v21
	v_cvt_pk_f16_f32 v2, v2, v3
	v_cvt_pk_f16_f32 v3, v4, v5
	s_waitcnt vmcnt(2)
	v_pk_add_f32 v[4:5], v[74:75], v[22:23]
	v_pk_add_f32 v[20:21], v[76:77], v[24:25]
	v_cvt_pk_f16_f32 v4, v4, v5
	v_cvt_pk_f16_f32 v5, v20, v21
	ds_write2_b64 v155, v[18:19], v[4:5] offset0:24 offset1:26
	v_pk_add_f32 v[4:5], v[74:75], v[6:7]
	v_pk_add_f32 v[6:7], v[76:77], v[8:9]
	v_cvt_pk_f16_f32 v4, v4, v5
	v_cvt_pk_f16_f32 v5, v6, v7
	ds_write2_b64 v176, v[2:3], v[4:5] offset0:88 offset1:90
	s_waitcnt vmcnt(1)
	v_pk_add_f32 v[2:3], v[78:79], v[26:27]
	v_pk_add_f32 v[4:5], v[80:81], v[28:29]
	v_cvt_pk_f16_f32 v2, v2, v3
	v_cvt_pk_f16_f32 v3, v4, v5
	v_pk_add_f32 v[4:5], v[78:79], v[10:11]
	v_pk_add_f32 v[6:7], v[80:81], v[12:13]
	v_pk_add_f32 v[44:45], v[68:69], v[64:65]
	v_cvt_pk_f16_f32 v4, v4, v5
	v_cvt_pk_f16_f32 v5, v6, v7
	s_waitcnt vmcnt(0)
	v_pk_add_f32 v[6:7], v[34:35], v[30:31]
	v_pk_add_f32 v[8:9], v[36:37], v[32:33]
	v_cvt_pk_f16_f32 v42, v42, v43
	v_cvt_pk_f16_f32 v43, v44, v45
	v_cvt_pk_f16_f32 v6, v6, v7
	v_cvt_pk_f16_f32 v7, v8, v9
	ds_write2_b64 v155, v[38:39], v[42:43] offset0:20 offset1:22
	v_pk_add_f32 v[38:39], v[66:67], v[46:47]
	v_pk_add_f32 v[42:43], v[68:69], v[48:49]
	ds_write2_b64 v155, v[2:3], v[6:7] offset0:28 offset1:30
	v_pk_add_f32 v[2:3], v[34:35], v[14:15]
	v_pk_add_f32 v[6:7], v[36:37], v[16:17]
	v_cvt_pk_f16_f32 v38, v38, v39
	v_cvt_pk_f16_f32 v39, v42, v43
	v_cvt_pk_f16_f32 v2, v2, v3
	v_cvt_pk_f16_f32 v3, v6, v7
	ds_write2_b64 v176, v[40:41], v[38:39] offset0:84 offset1:86
	ds_write2_b64 v176, v[4:5], v[2:3] offset0:92 offset1:94
	s_branch .Lepi_join
